# v051 + in-proj vT tile epilogue: the 8 bias loads hoisted to one batch at the epilogue start (7 full drains removed, result stores stay in flight)
# speedup vs baseline: 1.0157x; 1.0079x over previous
.LBB0_595:
	s_ashr_i32 s53, s52, 31
	s_lshl_b64 s[6:7], s[52:53], 19
	s_add_u32 s54, s16, s6
	s_addc_u32 s55, s17, s7
	s_and_b64 s[6:7], s[38:39], exec
	s_cselect_b32 s23, s55, s1
	s_cselect_b32 s53, s54, s0
	s_ashr_i32 s51, s50, 31
	s_lshl_b64 s[6:7], s[50:51], 19
	s_add_u32 s56, s14, s6
	s_addc_u32 s57, s15, s7
	s_and_b64 s[6:7], s[38:39], exec
	s_cselect_b32 s51, s57, s5
	s_cselect_b32 s69, s56, s4
	s_add_u32 s70, s4, 0x100
	v_mov_b32_e32 v2, 0
	s_addc_u32 s71, s5, 0
	s_mov_b32 s72, -2
	v_mov_b32_e32 v3, v2
	v_mov_b32_e32 v4, v2
	v_mov_b32_e32 v5, v2
	v_mov_b32_e32 v6, v2
	v_mov_b32_e32 v7, v2
	v_mov_b32_e32 v8, v2
	v_mov_b32_e32 v9, v2
	v_mov_b32_e32 v18, v2
	v_mov_b32_e32 v19, v2
	v_mov_b32_e32 v20, v2
	v_mov_b32_e32 v21, v2
	v_mov_b32_e32 v22, v2
	v_mov_b32_e32 v23, v2
	v_mov_b32_e32 v24, v2
	v_mov_b32_e32 v25, v2
	v_mov_b32_e32 v34, v2
	v_mov_b32_e32 v35, v2
	v_mov_b32_e32 v36, v2
	v_mov_b32_e32 v37, v2
	v_mov_b32_e32 v38, v2
	v_mov_b32_e32 v39, v2
	v_mov_b32_e32 v40, v2
	v_mov_b32_e32 v41, v2
	v_mov_b32_e32 v50, v2
	v_mov_b32_e32 v51, v2
	v_mov_b32_e32 v52, v2
	v_mov_b32_e32 v53, v2
	v_mov_b32_e32 v54, v2
	v_mov_b32_e32 v55, v2
	v_mov_b32_e32 v56, v2
	v_mov_b32_e32 v57, v2
	v_mov_b32_e32 v10, v2
	v_mov_b32_e32 v11, v2
	v_mov_b32_e32 v12, v2
	v_mov_b32_e32 v13, v2
	s_waitcnt vmcnt(16)
	v_mov_b32_e32 v14, v2
	v_mov_b32_e32 v15, v2
	v_mov_b32_e32 v16, v2
	v_mov_b32_e32 v17, v2
	v_mov_b32_e32 v26, v2
	v_mov_b32_e32 v27, v2
	v_mov_b32_e32 v28, v2
	v_mov_b32_e32 v29, v2
	v_mov_b32_e32 v30, v2
	v_mov_b32_e32 v31, v2
	v_mov_b32_e32 v32, v2
	v_mov_b32_e32 v33, v2
	v_mov_b32_e32 v42, v2
	v_mov_b32_e32 v43, v2
	v_mov_b32_e32 v44, v2
	v_mov_b32_e32 v45, v2
	v_mov_b32_e32 v46, v2
	v_mov_b32_e32 v47, v2
	v_mov_b32_e32 v48, v2
	v_mov_b32_e32 v49, v2
	v_mov_b32_e32 v58, v2
	v_mov_b32_e32 v59, v2
	v_mov_b32_e32 v60, v2
	v_mov_b32_e32 v61, v2
	v_mov_b32_e32 v62, v2
	v_mov_b32_e32 v63, v2
	v_mov_b32_e32 v64, v2
	v_mov_b32_e32 v65, v2
	v_mov_b32_e32 v66, v2
	v_mov_b32_e32 v67, v2
	v_mov_b32_e32 v68, v2
	v_mov_b32_e32 v69, v2
	v_mov_b32_e32 v70, v2
	v_mov_b32_e32 v71, v2
	v_mov_b32_e32 v72, v2
	v_mov_b32_e32 v73, v2
	v_mov_b32_e32 v82, v2
	v_mov_b32_e32 v83, v2
	v_mov_b32_e32 v84, v2
	v_mov_b32_e32 v85, v2
	v_mov_b32_e32 v86, v2
	v_mov_b32_e32 v87, v2
	v_mov_b32_e32 v88, v2
	v_mov_b32_e32 v89, v2
	v_mov_b32_e32 v98, v2
	v_mov_b32_e32 v99, v2
	v_mov_b32_e32 v100, v2
	v_mov_b32_e32 v101, v2
	v_mov_b32_e32 v102, v2
	v_mov_b32_e32 v103, v2
	v_mov_b32_e32 v104, v2
	v_mov_b32_e32 v105, v2
	v_mov_b32_e32 v114, v2
	v_mov_b32_e32 v115, v2
	v_mov_b32_e32 v116, v2
	v_mov_b32_e32 v117, v2
	v_mov_b32_e32 v118, v2
	v_mov_b32_e32 v119, v2
	v_mov_b32_e32 v120, v2
	v_mov_b32_e32 v121, v2
	v_mov_b32_e32 v74, v2
	v_mov_b32_e32 v75, v2
	v_mov_b32_e32 v76, v2
	v_mov_b32_e32 v77, v2
	v_mov_b32_e32 v78, v2
	v_mov_b32_e32 v79, v2
	v_mov_b32_e32 v80, v2
	v_mov_b32_e32 v81, v2
	v_mov_b32_e32 v90, v2
	v_mov_b32_e32 v91, v2
	v_mov_b32_e32 v92, v2
	v_mov_b32_e32 v93, v2
	v_mov_b32_e32 v94, v2
	v_mov_b32_e32 v95, v2
	v_mov_b32_e32 v96, v2
	v_mov_b32_e32 v97, v2
	v_mov_b32_e32 v106, v2
	v_mov_b32_e32 v107, v2
	v_mov_b32_e32 v108, v2
	v_mov_b32_e32 v109, v2
	v_mov_b32_e32 v110, v2
	v_mov_b32_e32 v111, v2
	v_mov_b32_e32 v112, v2
	v_mov_b32_e32 v113, v2
	v_mov_b32_e32 v122, v2
	v_mov_b32_e32 v123, v2
	v_mov_b32_e32 v124, v2
	v_mov_b32_e32 v125, v2
	v_mov_b32_e32 v126, v2
	v_mov_b32_e32 v127, v2
	v_mov_b32_e32 v128, v2
	v_mov_b32_e32 v129, v2

.LBB0_599:
	s_lshl_b32 s0, s67, 8
	s_lshl_b32 s1, s68, 1
	s_add_i32 s0, s0, s35
	s_or_b32 s1, s1, s65
	v_mov_b32_e32 v132, v0
	s_mul_hi_i32 s4, s1, 0xc00
	s_mulk_i32 s1, 0xc00
	s_ashr_i32 s5, s0, 31
	s_add_u32 s1, s1, s0
	v_and_b32_e32 v142, 15, v132
	v_and_or_b32 v130, v132, 7, s1
	v_lshlrev_b32_e32 v133, 3, v132
	v_lshrrev_b32_e32 v132, 1, v132
	v_and_b32_e32 v141, 24, v132
	v_or_b32_e32 v132, s0, v142
	v_and_b32_e32 v206, 64, v133
	v_ashrrev_i32_e32 v133, 31, v132
	v_lshl_add_u64 v[132:133], v[132:133], 2, s[44:45]
	global_load_dword v186, v[132:133], off
	global_load_dword v187, v[132:133], off offset:64
	global_load_dword v188, v[132:133], off offset:128
	global_load_dword v189, v[132:133], off offset:192
	global_load_dword v190, v[132:133], off offset:512
	global_load_dword v191, v[132:133], off offset:576
	global_load_dword v192, v[132:133], off offset:640
	global_load_dword v193, v[132:133], off offset:704
	s_addc_u32 s4, s4, s5
	v_mov_b32_e32 v131, s4
	v_lshlrev_b64 v[130:131], 8, v[130:131]
	v_lshl_add_u64 v[130:131], s[46:47], 0, v[130:131]
	v_lshl_add_u64 v[130:131], v[130:131], 0, v[206:207]
	v_lshlrev_b32_e32 v206, 1, v141
	v_lshl_add_u64 v[130:131], v[130:131], 0, v[206:207]
	s_movk_i32 s0, 0x1000
	s_waitcnt vmcnt(0)
	v_mov_b32_e32 v134, v186
	v_pk_add_f32 v[136:137], v[124:125], v[134:135] op_sel_hi:[1,0]
	v_pk_add_f32 v[124:125], v[122:123], v[134:135] op_sel_hi:[1,0]
	v_pk_add_f32 v[126:127], v[126:127], v[134:135] op_sel_hi:[1,0]
	v_mul_f32_e32 v123, 0x3d372713, v124
	v_fma_f32 v123, v124, v123, 1.0
	v_mul_f32_e32 v123, v124, v123
	v_mul_f32_e32 v123, 0xc0135761, v123
	v_exp_f32_e32 v123, v123
	v_mul_f32_e32 v122, 0x3d372713, v126
	v_fma_f32 v122, v126, v122, 1.0
	v_mul_f32_e32 v122, v126, v122
	v_add_f32_e32 v123, 1.0, v123
	v_rcp_f32_e32 v144, v123
	v_mul_f32_e32 v123, 0x3d372713, v127
	v_fma_f32 v123, v127, v123, 1.0
	v_mul_f32_e32 v123, v127, v123
	v_mul_f32_e32 v122, 0xc0135761, v122
	v_mul_f32_e32 v123, 0xc0135761, v123
	v_exp_f32_e32 v122, v122
	v_exp_f32_e32 v123, v123
	v_pk_add_f32 v[128:129], v[128:129], v[134:135] op_sel_hi:[1,0]
	v_pk_add_f32 v[118:119], v[118:119], v[134:135] op_sel_hi:[1,0]
	v_add_f32_e32 v122, 1.0, v122
	v_add_f32_e32 v123, 1.0, v123
	v_rcp_f32_e32 v122, v122
	v_rcp_f32_e32 v123, v123
	s_nop 0
	v_pk_mul_f32 v[122:123], v[126:127], v[122:123]
	v_mul_f32_e32 v126, 0x3d372713, v125
	v_fma_f32 v126, v125, v126, 1.0
	v_mul_f32_e32 v126, v125, v126
	v_mul_f32_e32 v126, 0xc0135761, v126
	v_exp_f32_e32 v126, v126
	v_mul_f32_e32 v127, 0x3d372713, v136
	v_fma_f32 v127, v136, v127, 1.0
	v_mul_f32_e32 v127, v136, v127
	v_mul_f32_e32 v127, 0xc0135761, v127
	v_add_f32_e32 v126, 1.0, v126
	v_exp_f32_e32 v127, v127
	v_rcp_f32_e32 v145, v126
	v_mul_f32_e32 v126, 0x3d372713, v128
	v_fma_f32 v126, v128, v126, 1.0
	v_add_f32_e32 v127, 1.0, v127
	v_pk_mul_f32 v[124:125], v[124:125], v[144:145]
	v_rcp_f32_e32 v144, v127
	v_mul_f32_e32 v127, 0x3d372713, v129
	v_fma_f32 v127, v129, v127, 1.0
	v_mul_f32_e32 v126, v128, v126
	v_mul_f32_e32 v127, v129, v127
	v_mul_f32_e32 v126, 0xc0135761, v126
	v_mul_f32_e32 v127, 0xc0135761, v127
	v_exp_f32_e32 v126, v126
	v_exp_f32_e32 v127, v127
	v_cvt_pk_bf16_f32 v146, v122, v123
	v_mov_b32_e32 v152, v146
	v_add_f32_e32 v126, 1.0, v126
	v_add_f32_e32 v127, 1.0, v127
	v_rcp_f32_e32 v126, v126
	v_rcp_f32_e32 v127, v127
	s_nop 0
	v_pk_mul_f32 v[126:127], v[128:129], v[126:127]
	v_mul_f32_e32 v128, 0x3d372713, v137
	v_fma_f32 v128, v137, v128, 1.0
	v_mul_f32_e32 v128, v137, v128
	v_mul_f32_e32 v128, 0xc0135761, v128
	v_exp_f32_e32 v128, v128
	s_nop 0
	v_add_f32_e32 v128, 1.0, v128
	v_rcp_f32_e32 v145, v128
	s_nop 0
	v_pk_mul_f32 v[128:129], v[136:137], v[144:145]
	v_pk_add_f32 v[136:137], v[120:121], v[134:135] op_sel_hi:[1,0]
	v_pk_add_f32 v[120:121], v[116:117], v[134:135] op_sel_hi:[1,0]
	v_pk_add_f32 v[116:117], v[114:115], v[134:135] op_sel_hi:[1,0]
	v_mul_f32_e32 v114, 0x3d372713, v118
	v_mul_f32_e32 v115, 0x3d372713, v116
	v_fma_f32 v115, v116, v115, 1.0
	v_mul_f32_e32 v115, v116, v115
	v_mul_f32_e32 v115, 0xc0135761, v115
	v_exp_f32_e32 v115, v115
	v_fma_f32 v114, v118, v114, 1.0
	v_mul_f32_e32 v114, v118, v114
	v_mul_f32_e32 v114, 0xc0135761, v114
	v_add_f32_e32 v115, 1.0, v115
	v_rcp_f32_e32 v148, v115
	v_mul_f32_e32 v115, 0x3d372713, v119
	v_fma_f32 v115, v119, v115, 1.0
	v_mul_f32_e32 v115, v119, v115
	v_mul_f32_e32 v115, 0xc0135761, v115
	v_exp_f32_e32 v114, v114
	v_exp_f32_e32 v115, v115
	v_mul_f32_e32 v134, 0x3d372713, v121
	v_fma_f32 v134, v121, v134, 1.0
	v_add_f32_e32 v114, 1.0, v114
	v_add_f32_e32 v115, 1.0, v115
	v_rcp_f32_e32 v114, v114
	v_rcp_f32_e32 v115, v115
	v_mul_f32_e32 v134, v121, v134
	v_mul_f32_e32 v134, 0xc0135761, v134
	v_exp_f32_e32 v134, v134
	v_pk_mul_f32 v[114:115], v[118:119], v[114:115]
	v_mul_f32_e32 v118, 0x3d372713, v117
	v_fma_f32 v118, v117, v118, 1.0
	v_mul_f32_e32 v118, v117, v118
	v_mul_f32_e32 v118, 0xc0135761, v118
	v_exp_f32_e32 v118, v118
	v_mul_f32_e32 v119, 0x3d372713, v120
	v_fma_f32 v119, v120, v119, 1.0
	v_mul_f32_e32 v119, v120, v119
	v_mul_f32_e32 v119, 0xc0135761, v119
	v_add_f32_e32 v118, 1.0, v118
	v_exp_f32_e32 v119, v119
	v_rcp_f32_e32 v149, v118
	v_mul_f32_e32 v118, 0x3d372713, v136
	v_fma_f32 v118, v136, v118, 1.0
	v_add_f32_e32 v119, 1.0, v119
	v_pk_mul_f32 v[116:117], v[116:117], v[148:149]
	v_rcp_f32_e32 v148, v119
	v_mul_f32_e32 v119, 0x3d372713, v137
	v_fma_f32 v119, v137, v119, 1.0
	v_mul_f32_e32 v118, v136, v118
	v_mul_f32_e32 v119, v137, v119
	v_mul_f32_e32 v118, 0xc0135761, v118
	v_mul_f32_e32 v119, 0xc0135761, v119
	v_exp_f32_e32 v118, v118
	v_exp_f32_e32 v119, v119
	v_add_f32_e32 v134, 1.0, v134
	v_rcp_f32_e32 v149, v134
	v_add_f32_e32 v118, 1.0, v118
	v_add_f32_e32 v119, 1.0, v119
	v_rcp_f32_e32 v118, v118
	v_rcp_f32_e32 v119, v119
	v_cvt_pk_bf16_f32 v145, v126, v127
	v_cvt_pk_bf16_f32 v144, v124, v125
	v_cvt_pk_bf16_f32 v143, v128, v129
	v_pk_mul_f32 v[118:119], v[136:137], v[118:119]
	v_pk_mul_f32 v[120:121], v[120:121], v[148:149]
	v_cvt_pk_bf16_f32 v148, v114, v115
	v_cvt_pk_bf16_f32 v149, v118, v119
	v_cvt_pk_bf16_f32 v150, v116, v117
	v_cvt_pk_bf16_f32 v151, v120, v121
	v_mov_b32_e32 v153, v145
	v_mov_b32_e32 v154, v144
	v_mov_b32_e32 v155, v143
	v_mov_b32_dpp v152, v148 row_ror:8 row_mask:0xf bank_mask:0xc
	v_mov_b32_dpp v153, v149 row_ror:8 row_mask:0xf bank_mask:0xc
	v_mov_b32_dpp v154, v150 row_ror:8 row_mask:0xf bank_mask:0xc
	v_mov_b32_dpp v155, v151 row_ror:8 row_mask:0xf bank_mask:0xc
	v_mov_b32_dpp v148, v146 row_ror:8 row_mask:0xf bank_mask:0x3
	v_mov_b32_dpp v149, v145 row_ror:8 row_mask:0xf bank_mask:0x3
	v_mov_b32_dpp v150, v144 row_ror:8 row_mask:0xf bank_mask:0x3
	v_mov_b32_dpp v151, v143 row_ror:8 row_mask:0xf bank_mask:0x3
	global_store_dwordx4 v[130:131], v[152:155], off
	global_store_dwordx4 v[130:131], v[148:151], off offset:2048
	s_nop 1
	v_mov_b32_e32 v134, v187
	v_pk_add_f32 v[106:107], v[106:107], v[134:135] op_sel_hi:[1,0]
	s_nop 0
	v_mul_f32_e32 v137, 0x3d372713, v106
	v_fma_f32 v137, v106, v137, 1.0
	v_mul_f32_e32 v137, v106, v137
	v_mul_f32_e32 v137, 0xc0135761, v137
	v_exp_f32_e32 v137, v137
	v_pk_add_f32 v[110:111], v[110:111], v[134:135] op_sel_hi:[1,0]
	v_pk_add_f32 v[108:109], v[108:109], v[134:135] op_sel_hi:[1,0]
	v_mul_f32_e32 v136, 0x3d372713, v110
	v_add_f32_e32 v137, 1.0, v137
	v_rcp_f32_e32 v144, v137
	v_mul_f32_e32 v137, 0x3d372713, v111
	v_fma_f32 v136, v110, v136, 1.0
	v_fma_f32 v137, v111, v137, 1.0
	v_mul_f32_e32 v136, v110, v136
	v_mul_f32_e32 v137, v111, v137
	v_mul_f32_e32 v136, 0xc0135761, v136
	v_mul_f32_e32 v137, 0xc0135761, v137
	v_exp_f32_e32 v136, v136
	v_exp_f32_e32 v137, v137
	v_pk_add_f32 v[112:113], v[112:113], v[134:135] op_sel_hi:[1,0]
	v_pk_add_f32 v[98:99], v[98:99], v[134:135] op_sel_hi:[1,0]
	v_add_f32_e32 v136, 1.0, v136
	v_add_f32_e32 v137, 1.0, v137
	v_rcp_f32_e32 v136, v136
	v_rcp_f32_e32 v137, v137
	v_pk_add_f32 v[102:103], v[102:103], v[134:135] op_sel_hi:[1,0]
	v_pk_add_f32 v[100:101], v[100:101], v[134:135] op_sel_hi:[1,0]
	v_pk_add_f32 v[104:105], v[104:105], v[134:135] op_sel_hi:[1,0]
	v_pk_mul_f32 v[136:137], v[110:111], v[136:137]
	v_mul_f32_e32 v110, 0x3d372713, v107
	v_fma_f32 v110, v107, v110, 1.0
	v_mul_f32_e32 v110, v107, v110
	v_mul_f32_e32 v110, 0xc0135761, v110
	v_exp_f32_e32 v110, v110
	s_nop 0
	v_add_f32_e32 v110, 1.0, v110
	v_rcp_f32_e32 v145, v110
	s_nop 0
	v_pk_mul_f32 v[144:145], v[106:107], v[144:145]
	v_mul_f32_e32 v107, 0x3d372713, v108
	v_fma_f32 v107, v108, v107, 1.0
	v_mul_f32_e32 v107, v108, v107
	v_mul_f32_e32 v107, 0xc0135761, v107
	v_exp_f32_e32 v107, v107
	v_mul_f32_e32 v106, 0x3d372713, v112
	v_fma_f32 v106, v112, v106, 1.0
	v_mul_f32_e32 v106, v112, v106
	v_add_f32_e32 v107, 1.0, v107
	v_rcp_f32_e32 v110, v107
	v_mul_f32_e32 v107, 0x3d372713, v113
	v_fma_f32 v107, v113, v107, 1.0
	v_mul_f32_e32 v107, v113, v107
	v_mul_f32_e32 v106, 0xc0135761, v106
	v_mul_f32_e32 v107, 0xc0135761, v107
	v_exp_f32_e32 v106, v106
	v_exp_f32_e32 v107, v107
	v_cvt_pk_bf16_f32 v143, v144, v145
	v_add_f32_e32 v106, 1.0, v106
	v_add_f32_e32 v107, 1.0, v107
	v_rcp_f32_e32 v106, v106
	v_rcp_f32_e32 v107, v107
	s_nop 0
	v_pk_mul_f32 v[146:147], v[112:113], v[106:107]
	v_mul_f32_e32 v106, 0x3d372713, v109
	v_fma_f32 v106, v109, v106, 1.0
	v_mul_f32_e32 v106, v109, v106
	v_mul_f32_e32 v106, 0xc0135761, v106
	v_exp_f32_e32 v106, v106
	v_pk_mul_f32 v[112:113], v[144:145], v[144:145]
	v_add_f32_e32 v106, 1.0, v106
	v_rcp_f32_e32 v111, v106
	v_pk_fma_f32 v[112:113], v[124:125], v[124:125], v[112:113]
	v_pk_mul_f32 v[106:107], v[146:147], v[146:147]
	v_pk_mul_f32 v[148:149], v[108:109], v[110:111]
	v_pk_mul_f32 v[108:109], v[136:137], v[136:137]
	v_pk_fma_f32 v[106:107], v[126:127], v[126:127], v[106:107]
	v_pk_fma_f32 v[108:109], v[122:123], v[122:123], v[108:109]
	v_mul_f32_e32 v123, 0x3d372713, v98
	v_fma_f32 v123, v98, v123, 1.0
	v_mul_f32_e32 v123, v98, v123
	v_mul_f32_e32 v123, 0xc0135761, v123
	v_exp_f32_e32 v123, v123
	v_mul_f32_e32 v122, 0x3d372713, v102
	v_fma_f32 v122, v102, v122, 1.0
	v_mul_f32_e32 v122, v102, v122
	v_add_f32_e32 v123, 1.0, v123
	v_rcp_f32_e32 v124, v123
	v_mul_f32_e32 v123, 0x3d372713, v103
	v_fma_f32 v123, v103, v123, 1.0
	v_mul_f32_e32 v123, v103, v123
	v_mul_f32_e32 v122, 0xc0135761, v122
	v_mul_f32_e32 v123, 0xc0135761, v123
	v_exp_f32_e32 v122, v122
	v_exp_f32_e32 v123, v123
	v_pk_mul_f32 v[110:111], v[148:149], v[148:149]
	v_cvt_pk_bf16_f32 v136, v136, v137
	v_add_f32_e32 v122, 1.0, v122
	v_add_f32_e32 v123, 1.0, v123
	v_rcp_f32_e32 v122, v122
	v_rcp_f32_e32 v123, v123
	v_pk_fma_f32 v[110:111], v[128:129], v[128:129], v[110:111]
	v_cvt_pk_bf16_f32 v137, v146, v147
	v_cvt_pk_bf16_f32 v144, v148, v149
	v_pk_mul_f32 v[122:123], v[102:103], v[122:123]
	v_mul_f32_e32 v102, 0x3d372713, v99
	v_fma_f32 v102, v99, v102, 1.0
	v_mul_f32_e32 v102, v99, v102
	v_mul_f32_e32 v102, 0xc0135761, v102
	v_exp_f32_e32 v102, v102
	s_nop 0
	v_add_f32_e32 v102, 1.0, v102
	v_rcp_f32_e32 v125, v102
	s_nop 0
	v_pk_mul_f32 v[124:125], v[98:99], v[124:125]
	v_mul_f32_e32 v99, 0x3d372713, v100
	v_fma_f32 v99, v100, v99, 1.0
	v_mul_f32_e32 v99, v100, v99
	v_mul_f32_e32 v99, 0xc0135761, v99
	v_exp_f32_e32 v99, v99
	v_mul_f32_e32 v98, 0x3d372713, v104
	v_fma_f32 v98, v104, v98, 1.0
	v_mul_f32_e32 v98, v104, v98
	v_add_f32_e32 v99, 1.0, v99
	v_rcp_f32_e32 v102, v99
	v_mul_f32_e32 v99, 0x3d372713, v105
	v_fma_f32 v99, v105, v99, 1.0
	v_mul_f32_e32 v99, v105, v99
	v_mul_f32_e32 v98, 0xc0135761, v98
	v_mul_f32_e32 v99, 0xc0135761, v99
	v_exp_f32_e32 v98, v98
	v_exp_f32_e32 v99, v99
	v_add_f32_e32 v98, 1.0, v98
	v_add_f32_e32 v99, 1.0, v99
	v_rcp_f32_e32 v98, v98
	v_rcp_f32_e32 v99, v99
	s_nop 0
	v_pk_mul_f32 v[126:127], v[104:105], v[98:99]
	v_mul_f32_e32 v98, 0x3d372713, v101
	v_fma_f32 v98, v101, v98, 1.0
	v_mul_f32_e32 v98, v101, v98
	v_mul_f32_e32 v98, 0xc0135761, v98
	v_exp_f32_e32 v98, v98
	v_pk_mul_f32 v[104:105], v[124:125], v[124:125]
	v_add_f32_e32 v98, 1.0, v98
	v_rcp_f32_e32 v103, v98
	v_pk_mul_f32 v[98:99], v[126:127], v[126:127]
	v_pk_fma_f32 v[104:105], v[116:117], v[116:117], v[104:105]
	v_pk_fma_f32 v[98:99], v[118:119], v[118:119], v[98:99]
	v_pk_mul_f32 v[128:129], v[100:101], v[102:103]
	v_cvt_pk_bf16_f32 v118, v124, v125
	v_add_co_u32_e32 v124, vcc, s0, v130
	v_pk_mul_f32 v[100:101], v[122:123], v[122:123]
	v_pk_mul_f32 v[102:103], v[128:129], v[128:129]
	v_addc_co_u32_e32 v125, vcc, 0, v131, vcc
	s_movk_i32 s0, 0x2000
	v_pk_fma_f32 v[100:101], v[114:115], v[114:115], v[100:101]
	v_pk_fma_f32 v[102:103], v[120:121], v[120:121], v[102:103]
	v_cvt_pk_bf16_f32 v116, v122, v123
	v_cvt_pk_bf16_f32 v117, v126, v127
	v_cvt_pk_bf16_f32 v119, v128, v129
	v_mov_b32_e32 v120, v136
	v_mov_b32_e32 v121, v137
	v_mov_b32_e32 v122, v143
	v_mov_b32_e32 v123, v144
	v_add_co_u32_e32 v114, vcc, s0, v130
	v_mov_b32_dpp v120, v116 row_ror:8 row_mask:0xf bank_mask:0xc
	v_mov_b32_dpp v121, v117 row_ror:8 row_mask:0xf bank_mask:0xc
	v_mov_b32_dpp v122, v118 row_ror:8 row_mask:0xf bank_mask:0xc
	v_mov_b32_dpp v123, v119 row_ror:8 row_mask:0xf bank_mask:0xc
	v_addc_co_u32_e32 v115, vcc, 0, v131, vcc
	v_mov_b32_dpp v116, v136 row_ror:8 row_mask:0xf bank_mask:0x3
	v_mov_b32_dpp v117, v137 row_ror:8 row_mask:0xf bank_mask:0x3
	v_mov_b32_dpp v118, v143 row_ror:8 row_mask:0xf bank_mask:0x3
	v_mov_b32_dpp v119, v144 row_ror:8 row_mask:0xf bank_mask:0x3
	global_store_dwordx4 v[114:115], v[120:123], off offset:-4096
	global_store_dwordx4 v[124:125], v[116:119], off offset:2048
	s_nop 1
	v_mov_b32_e32 v116, v188
	s_movk_i32 s0, 0x3000
	v_pk_add_f32 v[94:95], v[94:95], v[116:117] op_sel_hi:[1,0]
	v_pk_add_f32 v[96:97], v[96:97], v[116:117] op_sel_hi:[1,0]
	v_pk_add_f32 v[92:93], v[92:93], v[116:117] op_sel_hi:[1,0]
	v_pk_add_f32 v[90:91], v[90:91], v[116:117] op_sel_hi:[1,0]
	v_mul_f32_e32 v117, 0x3d372713, v94
	v_fma_f32 v117, v94, v117, 1.0
	v_mul_f32_e32 v117, v94, v117
	v_mul_f32_e32 v117, 0xc0135761, v117
	v_exp_f32_e32 v117, v117
	s_nop 0
	v_add_f32_e32 v117, 1.0, v117
	v_rcp_f32_e32 v118, v117
	v_mul_f32_e32 v117, 0x3d372713, v90
	v_fma_f32 v117, v90, v117, 1.0
	v_mul_f32_e32 v117, v90, v117
	v_mul_f32_e32 v117, 0xc0135761, v117
	v_exp_f32_e32 v117, v117
	s_nop 0
	v_add_f32_e32 v117, 1.0, v117
	v_rcp_f32_e32 v120, v117
	v_mul_f32_e32 v117, 0x3d372713, v95
	v_fma_f32 v117, v95, v117, 1.0
	v_mul_f32_e32 v117, v95, v117
	v_mul_f32_e32 v117, 0xc0135761, v117
	v_exp_f32_e32 v117, v117
	s_nop 0
	v_add_f32_e32 v117, 1.0, v117
	v_rcp_f32_e32 v119, v117
	s_nop 0
	v_pk_mul_f32 v[118:119], v[94:95], v[118:119]
	v_mul_f32_e32 v94, 0x3d372713, v91
	v_fma_f32 v94, v91, v94, 1.0
	v_mul_f32_e32 v94, v91, v94
	v_mul_f32_e32 v94, 0xc0135761, v94
	v_exp_f32_e32 v94, v94
	v_cvt_pk_bf16_f32 v117, v118, v119
	v_pk_add_f32 v[82:83], v[82:83], v[116:117] op_sel_hi:[1,0]
	v_pk_add_f32 v[86:87], v[86:87], v[116:117] op_sel_hi:[1,0]
	v_add_f32_e32 v94, 1.0, v94
	v_rcp_f32_e32 v121, v94
	v_pk_add_f32 v[84:85], v[84:85], v[116:117] op_sel_hi:[1,0]
	v_pk_add_f32 v[88:89], v[88:89], v[116:117] op_sel_hi:[1,0]
	v_pk_mul_f32 v[120:121], v[90:91], v[120:121]
	v_mul_f32_e32 v91, 0x3d372713, v92
	v_fma_f32 v91, v92, v91, 1.0
	v_mul_f32_e32 v91, v92, v91
	v_mul_f32_e32 v91, 0xc0135761, v91
	v_exp_f32_e32 v91, v91
	v_mul_f32_e32 v90, 0x3d372713, v96
	v_fma_f32 v90, v96, v90, 1.0
	v_mul_f32_e32 v90, v96, v90
	v_add_f32_e32 v91, 1.0, v91
	v_rcp_f32_e32 v94, v91
	v_mul_f32_e32 v91, 0x3d372713, v97
	v_fma_f32 v91, v97, v91, 1.0
	v_mul_f32_e32 v91, v97, v91
	v_mul_f32_e32 v90, 0xc0135761, v90
	v_mul_f32_e32 v91, 0xc0135761, v91
	v_exp_f32_e32 v90, v90
	v_exp_f32_e32 v91, v91
	v_add_f32_e32 v90, 1.0, v90
	v_add_f32_e32 v91, 1.0, v91
	v_rcp_f32_e32 v90, v90
	v_rcp_f32_e32 v91, v91
	s_nop 0
	v_pk_mul_f32 v[122:123], v[96:97], v[90:91]
	v_mul_f32_e32 v90, 0x3d372713, v93
	v_fma_f32 v90, v93, v90, 1.0
	v_mul_f32_e32 v90, v93, v90
	v_mul_f32_e32 v90, 0xc0135761, v90
	v_exp_f32_e32 v90, v90
	s_nop 0
	v_add_f32_e32 v90, 1.0, v90
	v_rcp_f32_e32 v95, v90
	v_pk_fma_f32 v[90:91], v[118:119], v[118:119], v[108:109]
	v_cvt_pk_bf16_f32 v118, v122, v123
	v_cvt_pk_bf16_f32 v119, v120, v121
	v_pk_mul_f32 v[124:125], v[92:93], v[94:95]
	v_pk_fma_f32 v[94:95], v[122:123], v[122:123], v[106:107]
	v_mul_f32_e32 v107, 0x3d372713, v82
	v_fma_f32 v107, v82, v107, 1.0
	v_mul_f32_e32 v107, v82, v107
	v_mul_f32_e32 v107, 0xc0135761, v107
	v_exp_f32_e32 v107, v107
	v_mul_f32_e32 v106, 0x3d372713, v86
	v_fma_f32 v106, v86, v106, 1.0
	v_mul_f32_e32 v106, v86, v106
	v_add_f32_e32 v107, 1.0, v107
	v_rcp_f32_e32 v108, v107
	v_mul_f32_e32 v107, 0x3d372713, v87
	v_fma_f32 v107, v87, v107, 1.0
	v_mul_f32_e32 v107, v87, v107
	v_mul_f32_e32 v106, 0xc0135761, v106
	v_mul_f32_e32 v107, 0xc0135761, v107
	v_exp_f32_e32 v106, v106
	v_exp_f32_e32 v107, v107
	v_pk_fma_f32 v[96:97], v[124:125], v[124:125], v[110:111]
	v_pk_fma_f32 v[92:93], v[120:121], v[120:121], v[112:113]
	v_add_f32_e32 v106, 1.0, v106
	v_add_f32_e32 v107, 1.0, v107
	v_rcp_f32_e32 v106, v106
	v_rcp_f32_e32 v107, v107
	v_cvt_pk_bf16_f32 v120, v124, v125
	v_pk_mul_f32 v[106:107], v[86:87], v[106:107]
	v_mul_f32_e32 v86, 0x3d372713, v83
	v_fma_f32 v86, v83, v86, 1.0
	v_mul_f32_e32 v86, v83, v86
	v_mul_f32_e32 v86, 0xc0135761, v86
	v_exp_f32_e32 v86, v86
	s_nop 0
	v_add_f32_e32 v86, 1.0, v86
	v_rcp_f32_e32 v109, v86
	s_nop 0
	v_pk_mul_f32 v[108:109], v[82:83], v[108:109]
	v_mul_f32_e32 v83, 0x3d372713, v84
	v_fma_f32 v83, v84, v83, 1.0
	v_mul_f32_e32 v83, v84, v83
	v_mul_f32_e32 v83, 0xc0135761, v83
	v_exp_f32_e32 v83, v83
	v_mul_f32_e32 v82, 0x3d372713, v88
	v_fma_f32 v82, v88, v82, 1.0
	v_mul_f32_e32 v82, v88, v82
	v_add_f32_e32 v83, 1.0, v83
	v_rcp_f32_e32 v86, v83
	v_mul_f32_e32 v83, 0x3d372713, v89
	v_fma_f32 v83, v89, v83, 1.0
	v_mul_f32_e32 v83, v89, v83
	v_mul_f32_e32 v82, 0xc0135761, v82
	v_mul_f32_e32 v83, 0xc0135761, v83
	v_exp_f32_e32 v82, v82
	v_exp_f32_e32 v83, v83
	v_add_f32_e32 v82, 1.0, v82
	v_add_f32_e32 v83, 1.0, v83
	v_rcp_f32_e32 v82, v82
	v_rcp_f32_e32 v83, v83
	s_nop 0
	v_pk_mul_f32 v[110:111], v[88:89], v[82:83]
	v_mul_f32_e32 v82, 0x3d372713, v85
	v_fma_f32 v82, v85, v82, 1.0
	v_mul_f32_e32 v82, v85, v82
	v_mul_f32_e32 v82, 0xc0135761, v82
	v_exp_f32_e32 v82, v82
	s_nop 0
	v_add_f32_e32 v82, 1.0, v82
	v_rcp_f32_e32 v87, v82
	v_pk_fma_f32 v[82:83], v[106:107], v[106:107], v[100:101]
	v_cvt_pk_bf16_f32 v100, v108, v109
	v_pk_mul_f32 v[112:113], v[84:85], v[86:87]
	v_pk_fma_f32 v[86:87], v[110:111], v[110:111], v[98:99]
	v_pk_fma_f32 v[84:85], v[108:109], v[108:109], v[104:105]
	v_pk_fma_f32 v[88:89], v[112:113], v[112:113], v[102:103]
	v_cvt_pk_bf16_f32 v98, v106, v107
	v_cvt_pk_bf16_f32 v99, v110, v111
	v_cvt_pk_bf16_f32 v101, v112, v113
	v_mov_b32_e32 v102, v117
	v_mov_b32_e32 v103, v118
	v_mov_b32_e32 v104, v119
	v_mov_b32_e32 v105, v120
	v_mov_b32_dpp v102, v98 row_ror:8 row_mask:0xf bank_mask:0xc
	v_mov_b32_dpp v103, v99 row_ror:8 row_mask:0xf bank_mask:0xc
	v_mov_b32_dpp v104, v100 row_ror:8 row_mask:0xf bank_mask:0xc
	v_mov_b32_dpp v105, v101 row_ror:8 row_mask:0xf bank_mask:0xc
	v_mov_b32_dpp v98, v117 row_ror:8 row_mask:0xf bank_mask:0x3
	v_mov_b32_dpp v99, v118 row_ror:8 row_mask:0xf bank_mask:0x3
	v_mov_b32_dpp v100, v119 row_ror:8 row_mask:0xf bank_mask:0x3
	v_mov_b32_dpp v101, v120 row_ror:8 row_mask:0xf bank_mask:0x3
	global_store_dwordx4 v[114:115], v[102:105], off
	global_store_dwordx4 v[114:115], v[98:101], off offset:2048
	s_nop 1
	v_mov_b32_e32 v98, v189
	v_pk_add_f32 v[78:79], v[78:79], v[98:99] op_sel_hi:[1,0]
	v_pk_add_f32 v[80:81], v[80:81], v[98:99] op_sel_hi:[1,0]
	v_pk_add_f32 v[76:77], v[76:77], v[98:99] op_sel_hi:[1,0]
	v_pk_add_f32 v[74:75], v[74:75], v[98:99] op_sel_hi:[1,0]
	v_mul_f32_e32 v99, 0x3d372713, v78
	v_fma_f32 v99, v78, v99, 1.0
	v_mul_f32_e32 v99, v78, v99
	v_mul_f32_e32 v99, 0xc0135761, v99
	v_exp_f32_e32 v99, v99
	s_nop 0
	v_add_f32_e32 v99, 1.0, v99
	v_rcp_f32_e32 v100, v99
	v_mul_f32_e32 v99, 0x3d372713, v74
	v_fma_f32 v99, v74, v99, 1.0
	v_mul_f32_e32 v99, v74, v99
	v_mul_f32_e32 v99, 0xc0135761, v99
	v_exp_f32_e32 v99, v99
	s_nop 0
	v_add_f32_e32 v99, 1.0, v99
	v_rcp_f32_e32 v102, v99
	v_mul_f32_e32 v99, 0x3d372713, v79
	v_fma_f32 v99, v79, v99, 1.0
	v_mul_f32_e32 v99, v79, v99
	v_mul_f32_e32 v99, 0xc0135761, v99
	v_exp_f32_e32 v99, v99
	s_nop 0
	v_add_f32_e32 v99, 1.0, v99
	v_rcp_f32_e32 v101, v99
	s_nop 0
	v_pk_mul_f32 v[100:101], v[78:79], v[100:101]
	v_mul_f32_e32 v78, 0x3d372713, v75
	v_fma_f32 v78, v75, v78, 1.0
	v_mul_f32_e32 v78, v75, v78
	v_mul_f32_e32 v78, 0xc0135761, v78
	v_exp_f32_e32 v78, v78
	v_cvt_pk_bf16_f32 v99, v100, v101
	v_pk_add_f32 v[66:67], v[66:67], v[98:99] op_sel_hi:[1,0]
	v_pk_add_f32 v[70:71], v[70:71], v[98:99] op_sel_hi:[1,0]
	v_add_f32_e32 v78, 1.0, v78
	v_rcp_f32_e32 v103, v78
	v_pk_add_f32 v[68:69], v[68:69], v[98:99] op_sel_hi:[1,0]
	v_pk_add_f32 v[72:73], v[72:73], v[98:99] op_sel_hi:[1,0]
	v_pk_mul_f32 v[102:103], v[74:75], v[102:103]
	v_mul_f32_e32 v75, 0x3d372713, v76
	v_fma_f32 v75, v76, v75, 1.0
	v_mul_f32_e32 v75, v76, v75
	v_mul_f32_e32 v75, 0xc0135761, v75
	v_exp_f32_e32 v75, v75
	v_mul_f32_e32 v74, 0x3d372713, v80
	v_fma_f32 v74, v80, v74, 1.0
	v_mul_f32_e32 v74, v80, v74
	v_add_f32_e32 v75, 1.0, v75
	v_rcp_f32_e32 v78, v75
	v_mul_f32_e32 v75, 0x3d372713, v81
	v_fma_f32 v75, v81, v75, 1.0
	v_mul_f32_e32 v75, v81, v75
	v_mul_f32_e32 v74, 0xc0135761, v74
	v_mul_f32_e32 v75, 0xc0135761, v75
	v_exp_f32_e32 v74, v74
	v_exp_f32_e32 v75, v75
	v_add_f32_e32 v74, 1.0, v74
	v_add_f32_e32 v75, 1.0, v75
	v_rcp_f32_e32 v74, v74
	v_rcp_f32_e32 v75, v75
	s_nop 0
	v_pk_mul_f32 v[104:105], v[80:81], v[74:75]
	v_mul_f32_e32 v74, 0x3d372713, v77
	v_fma_f32 v74, v77, v74, 1.0
	v_mul_f32_e32 v74, v77, v74
	v_mul_f32_e32 v74, 0xc0135761, v74
	v_exp_f32_e32 v74, v74
	v_pk_fma_f32 v[80:81], v[102:103], v[102:103], v[92:93]
	v_add_f32_e32 v74, 1.0, v74
	v_rcp_f32_e32 v79, v74
	v_pk_fma_f32 v[74:75], v[104:105], v[104:105], v[94:95]
	v_pk_mul_f32 v[106:107], v[76:77], v[78:79]
	v_pk_fma_f32 v[78:79], v[100:101], v[100:101], v[90:91]
	v_mul_f32_e32 v91, 0x3d372713, v66
	v_fma_f32 v91, v66, v91, 1.0
	v_mul_f32_e32 v91, v66, v91
	v_mul_f32_e32 v91, 0xc0135761, v91
	v_exp_f32_e32 v91, v91
	v_mul_f32_e32 v90, 0x3d372713, v70
	v_fma_f32 v90, v70, v90, 1.0
	v_mul_f32_e32 v90, v70, v90
	v_add_f32_e32 v91, 1.0, v91
	v_rcp_f32_e32 v92, v91
	v_mul_f32_e32 v91, 0x3d372713, v71
	v_fma_f32 v91, v71, v91, 1.0
	v_mul_f32_e32 v91, v71, v91
	v_mul_f32_e32 v90, 0xc0135761, v90
	v_mul_f32_e32 v91, 0xc0135761, v91
	v_exp_f32_e32 v90, v90
	v_exp_f32_e32 v91, v91
	v_pk_fma_f32 v[76:77], v[106:107], v[106:107], v[96:97]
	v_cvt_pk_bf16_f32 v100, v104, v105
	v_add_f32_e32 v90, 1.0, v90
	v_add_f32_e32 v91, 1.0, v91
	v_rcp_f32_e32 v90, v90
	v_rcp_f32_e32 v91, v91
	v_cvt_pk_bf16_f32 v101, v102, v103
	v_cvt_pk_bf16_f32 v102, v106, v107
	v_pk_mul_f32 v[90:91], v[70:71], v[90:91]
	v_mul_f32_e32 v70, 0x3d372713, v67
	v_fma_f32 v70, v67, v70, 1.0
	v_mul_f32_e32 v70, v67, v70
	v_mul_f32_e32 v70, 0xc0135761, v70
	v_exp_f32_e32 v70, v70
	s_nop 0
	v_add_f32_e32 v70, 1.0, v70
	v_rcp_f32_e32 v93, v70
	s_nop 0
	v_pk_mul_f32 v[92:93], v[66:67], v[92:93]
	v_mul_f32_e32 v67, 0x3d372713, v68
	v_fma_f32 v67, v68, v67, 1.0
	v_mul_f32_e32 v67, v68, v67
	v_mul_f32_e32 v67, 0xc0135761, v67
	v_exp_f32_e32 v67, v67
	v_mul_f32_e32 v66, 0x3d372713, v72
	v_fma_f32 v66, v72, v66, 1.0
	v_mul_f32_e32 v66, v72, v66
	v_add_f32_e32 v67, 1.0, v67
	v_rcp_f32_e32 v70, v67
	v_mul_f32_e32 v67, 0x3d372713, v73
	v_fma_f32 v67, v73, v67, 1.0
	v_mul_f32_e32 v67, v73, v67
	v_mul_f32_e32 v66, 0xc0135761, v66
	v_mul_f32_e32 v67, 0xc0135761, v67
	v_exp_f32_e32 v66, v66
	v_exp_f32_e32 v67, v67
	v_add_f32_e32 v66, 1.0, v66
	v_add_f32_e32 v67, 1.0, v67
	v_rcp_f32_e32 v66, v66
	v_rcp_f32_e32 v67, v67
	s_nop 0
	v_pk_mul_f32 v[94:95], v[72:73], v[66:67]
	v_mul_f32_e32 v66, 0x3d372713, v69
	v_fma_f32 v66, v69, v66, 1.0
	v_mul_f32_e32 v66, v69, v66
	v_mul_f32_e32 v66, 0xc0135761, v66
	v_exp_f32_e32 v66, v66
	v_pk_fma_f32 v[72:73], v[92:93], v[92:93], v[84:85]
	v_cvt_pk_bf16_f32 v84, v92, v93
	v_add_f32_e32 v66, 1.0, v66
	v_rcp_f32_e32 v71, v66
	v_pk_fma_f32 v[66:67], v[94:95], v[94:95], v[86:87]
	v_mov_b32_e32 v86, v99
	v_mov_b32_e32 v87, v100
	v_pk_mul_f32 v[96:97], v[68:69], v[70:71]
	v_pk_fma_f32 v[70:71], v[90:91], v[90:91], v[82:83]
	v_pk_fma_f32 v[68:69], v[96:97], v[96:97], v[88:89]
	v_cvt_pk_bf16_f32 v82, v90, v91
	v_cvt_pk_bf16_f32 v83, v94, v95
	v_cvt_pk_bf16_f32 v85, v96, v97
	v_mov_b32_e32 v88, v101
	v_mov_b32_e32 v89, v102
	v_add_co_u32_e32 v90, vcc, s0, v130
	v_mov_b32_dpp v86, v82 row_ror:8 row_mask:0xf bank_mask:0xc
	v_mov_b32_dpp v87, v83 row_ror:8 row_mask:0xf bank_mask:0xc
	v_mov_b32_dpp v88, v84 row_ror:8 row_mask:0xf bank_mask:0xc
	v_mov_b32_dpp v89, v85 row_ror:8 row_mask:0xf bank_mask:0xc
	v_addc_co_u32_e32 v91, vcc, 0, v131, vcc
	v_mov_b32_dpp v82, v99 row_ror:8 row_mask:0xf bank_mask:0x3
	v_mov_b32_dpp v83, v100 row_ror:8 row_mask:0xf bank_mask:0x3
	v_mov_b32_dpp v84, v101 row_ror:8 row_mask:0xf bank_mask:0x3
	v_mov_b32_dpp v85, v102 row_ror:8 row_mask:0xf bank_mask:0x3
	global_store_dwordx4 v[90:91], v[86:89], off
	global_store_dwordx4 v[90:91], v[82:85], off offset:2048
	s_nop 1
	v_mov_b32_e32 v82, v190
	s_mov_b32 s0, 0x8000
	v_pk_add_f32 v[62:63], v[62:63], v[82:83] op_sel_hi:[1,0]
	v_pk_add_f32 v[64:65], v[64:65], v[82:83] op_sel_hi:[1,0]
	v_pk_add_f32 v[60:61], v[60:61], v[82:83] op_sel_hi:[1,0]
	v_pk_add_f32 v[58:59], v[58:59], v[82:83] op_sel_hi:[1,0]
	v_mul_f32_e32 v83, 0x3d372713, v62
	v_fma_f32 v83, v62, v83, 1.0
	v_mul_f32_e32 v83, v62, v83
	v_mul_f32_e32 v83, 0xc0135761, v83
	v_exp_f32_e32 v83, v83
	s_nop 0
	v_add_f32_e32 v83, 1.0, v83
	v_rcp_f32_e32 v84, v83
	v_mul_f32_e32 v83, 0x3d372713, v58
	v_fma_f32 v83, v58, v83, 1.0
	v_mul_f32_e32 v83, v58, v83
	v_mul_f32_e32 v83, 0xc0135761, v83
	v_exp_f32_e32 v83, v83
	s_nop 0
	v_add_f32_e32 v83, 1.0, v83
	v_rcp_f32_e32 v86, v83
	v_mul_f32_e32 v83, 0x3d372713, v63
	v_fma_f32 v83, v63, v83, 1.0
	v_mul_f32_e32 v83, v63, v83
	v_mul_f32_e32 v83, 0xc0135761, v83
	v_exp_f32_e32 v83, v83
	s_nop 0
	v_add_f32_e32 v83, 1.0, v83
	v_rcp_f32_e32 v85, v83
	s_nop 0
	v_pk_mul_f32 v[84:85], v[62:63], v[84:85]
	v_mul_f32_e32 v62, 0x3d372713, v59
	v_fma_f32 v62, v59, v62, 1.0
	v_mul_f32_e32 v62, v59, v62
	v_mul_f32_e32 v62, 0xc0135761, v62
	v_exp_f32_e32 v62, v62
	v_cvt_pk_bf16_f32 v83, v84, v85
	v_pk_add_f32 v[50:51], v[50:51], v[82:83] op_sel_hi:[1,0]
	v_pk_add_f32 v[54:55], v[54:55], v[82:83] op_sel_hi:[1,0]
	v_add_f32_e32 v62, 1.0, v62
	v_rcp_f32_e32 v87, v62
	v_pk_add_f32 v[52:53], v[52:53], v[82:83] op_sel_hi:[1,0]
	v_pk_add_f32 v[56:57], v[56:57], v[82:83] op_sel_hi:[1,0]
	v_pk_mul_f32 v[86:87], v[58:59], v[86:87]
	v_mul_f32_e32 v59, 0x3d372713, v60
	v_fma_f32 v59, v60, v59, 1.0
	v_mul_f32_e32 v59, v60, v59
	v_mul_f32_e32 v59, 0xc0135761, v59
	v_exp_f32_e32 v59, v59
	v_mul_f32_e32 v58, 0x3d372713, v64
	v_fma_f32 v58, v64, v58, 1.0
	v_mul_f32_e32 v58, v64, v58
	v_add_f32_e32 v59, 1.0, v59
	v_rcp_f32_e32 v62, v59
	v_mul_f32_e32 v59, 0x3d372713, v65
	v_fma_f32 v59, v65, v59, 1.0
	v_mul_f32_e32 v59, v65, v59
	v_mul_f32_e32 v58, 0xc0135761, v58
	v_mul_f32_e32 v59, 0xc0135761, v59
	v_exp_f32_e32 v58, v58
	v_exp_f32_e32 v59, v59
	v_add_f32_e32 v58, 1.0, v58
	v_add_f32_e32 v59, 1.0, v59
	v_rcp_f32_e32 v58, v58
	v_rcp_f32_e32 v59, v59
	s_nop 0
	v_pk_mul_f32 v[88:89], v[64:65], v[58:59]
	v_mul_f32_e32 v58, 0x3d372713, v61
	v_fma_f32 v58, v61, v58, 1.0
	v_mul_f32_e32 v58, v61, v58
	v_mul_f32_e32 v58, 0xc0135761, v58
	v_exp_f32_e32 v58, v58
	s_nop 0
	v_add_f32_e32 v58, 1.0, v58
	v_rcp_f32_e32 v63, v58
	v_pk_fma_f32 v[58:59], v[84:85], v[84:85], v[78:79]
	v_cvt_pk_bf16_f32 v84, v88, v89
	v_cvt_pk_bf16_f32 v85, v86, v87
	v_pk_mul_f32 v[90:91], v[60:61], v[62:63]
	v_pk_fma_f32 v[62:63], v[88:89], v[88:89], v[74:75]
	v_mul_f32_e32 v75, 0x3d372713, v50
	v_fma_f32 v75, v50, v75, 1.0
	v_mul_f32_e32 v75, v50, v75
	v_mul_f32_e32 v75, 0xc0135761, v75
	v_exp_f32_e32 v75, v75
	v_pk_fma_f32 v[64:65], v[90:91], v[90:91], v[76:77]
	v_mul_f32_e32 v74, 0x3d372713, v54
	v_fma_f32 v74, v54, v74, 1.0
	v_add_f32_e32 v75, 1.0, v75
	v_rcp_f32_e32 v76, v75
	v_mul_f32_e32 v75, 0x3d372713, v55
	v_fma_f32 v75, v55, v75, 1.0
	v_mul_f32_e32 v74, v54, v74
	v_mul_f32_e32 v75, v55, v75
	v_mul_f32_e32 v74, 0xc0135761, v74
	v_mul_f32_e32 v75, 0xc0135761, v75
	v_exp_f32_e32 v74, v74
	v_exp_f32_e32 v75, v75
	v_pk_fma_f32 v[60:61], v[86:87], v[86:87], v[80:81]
	v_cvt_pk_bf16_f32 v86, v90, v91
	v_add_f32_e32 v74, 1.0, v74
	v_add_f32_e32 v75, 1.0, v75
	v_rcp_f32_e32 v74, v74
	v_rcp_f32_e32 v75, v75
	s_nop 0
	v_pk_mul_f32 v[74:75], v[54:55], v[74:75]
	v_mul_f32_e32 v54, 0x3d372713, v51
	v_fma_f32 v54, v51, v54, 1.0
	v_mul_f32_e32 v54, v51, v54
	v_mul_f32_e32 v54, 0xc0135761, v54
	v_exp_f32_e32 v54, v54
	s_nop 0
	v_add_f32_e32 v54, 1.0, v54
	v_rcp_f32_e32 v77, v54
	s_nop 0
	v_pk_mul_f32 v[76:77], v[50:51], v[76:77]
	v_mul_f32_e32 v51, 0x3d372713, v52
	v_fma_f32 v51, v52, v51, 1.0
	v_mul_f32_e32 v51, v52, v51
	v_mul_f32_e32 v51, 0xc0135761, v51
	v_exp_f32_e32 v51, v51
	v_mul_f32_e32 v50, 0x3d372713, v56
	v_fma_f32 v50, v56, v50, 1.0
	v_mul_f32_e32 v50, v56, v50
	v_add_f32_e32 v51, 1.0, v51
	v_rcp_f32_e32 v54, v51
	v_mul_f32_e32 v51, 0x3d372713, v57
	v_fma_f32 v51, v57, v51, 1.0
	v_mul_f32_e32 v51, v57, v51
	v_mul_f32_e32 v50, 0xc0135761, v50
	v_mul_f32_e32 v51, 0xc0135761, v51
	v_exp_f32_e32 v50, v50
	v_exp_f32_e32 v51, v51
	v_add_f32_e32 v50, 1.0, v50
	v_add_f32_e32 v51, 1.0, v51
	v_rcp_f32_e32 v50, v50
	v_rcp_f32_e32 v51, v51
	s_nop 0
	v_pk_mul_f32 v[78:79], v[56:57], v[50:51]
	v_mul_f32_e32 v50, 0x3d372713, v53
	v_fma_f32 v50, v53, v50, 1.0
	v_mul_f32_e32 v50, v53, v50
	v_mul_f32_e32 v50, 0xc0135761, v50
	v_exp_f32_e32 v50, v50
	s_nop 0
	v_add_f32_e32 v50, 1.0, v50
	v_rcp_f32_e32 v55, v50
	v_pk_fma_f32 v[50:51], v[74:75], v[74:75], v[70:71]
	v_cvt_pk_bf16_f32 v70, v76, v77
	v_pk_mul_f32 v[80:81], v[52:53], v[54:55]
	v_pk_fma_f32 v[52:53], v[76:77], v[76:77], v[72:73]
	v_add_co_u32_e32 v76, vcc, s0, v130
	s_mov_b32 s0, 0x9000
	s_nop 0
	v_addc_co_u32_e32 v77, vcc, 0, v131, vcc
	v_pk_fma_f32 v[54:55], v[78:79], v[78:79], v[66:67]
	v_pk_fma_f32 v[56:57], v[80:81], v[80:81], v[68:69]
	v_cvt_pk_bf16_f32 v68, v74, v75
	v_cvt_pk_bf16_f32 v69, v78, v79
	v_cvt_pk_bf16_f32 v71, v80, v81
	v_mov_b32_e32 v72, v83
	v_mov_b32_e32 v73, v84
	v_mov_b32_e32 v74, v85
	v_mov_b32_e32 v75, v86
	v_add_co_u32_e32 v66, vcc, s0, v130
	v_mov_b32_dpp v72, v68 row_ror:8 row_mask:0xf bank_mask:0xc
	v_mov_b32_dpp v73, v69 row_ror:8 row_mask:0xf bank_mask:0xc
	v_mov_b32_dpp v74, v70 row_ror:8 row_mask:0xf bank_mask:0xc
	v_mov_b32_dpp v75, v71 row_ror:8 row_mask:0xf bank_mask:0xc
	v_addc_co_u32_e32 v67, vcc, 0, v131, vcc
	v_mov_b32_dpp v68, v83 row_ror:8 row_mask:0xf bank_mask:0x3
	v_mov_b32_dpp v69, v84 row_ror:8 row_mask:0xf bank_mask:0x3
	v_mov_b32_dpp v70, v85 row_ror:8 row_mask:0xf bank_mask:0x3
	v_mov_b32_dpp v71, v86 row_ror:8 row_mask:0xf bank_mask:0x3
	global_store_dwordx4 v[66:67], v[72:75], off offset:-4096
	global_store_dwordx4 v[76:77], v[68:71], off offset:2048
	s_nop 1
	v_mov_b32_e32 v68, v191
	s_mov_b32 s0, 0xa000
	v_pk_add_f32 v[46:47], v[46:47], v[68:69] op_sel_hi:[1,0]
	v_pk_add_f32 v[48:49], v[48:49], v[68:69] op_sel_hi:[1,0]
	v_pk_add_f32 v[44:45], v[44:45], v[68:69] op_sel_hi:[1,0]
	v_pk_add_f32 v[42:43], v[42:43], v[68:69] op_sel_hi:[1,0]
	v_mul_f32_e32 v69, 0x3d372713, v46
	v_fma_f32 v69, v46, v69, 1.0
	v_mul_f32_e32 v69, v46, v69
	v_mul_f32_e32 v69, 0xc0135761, v69
	v_exp_f32_e32 v69, v69
	s_nop 0
	v_add_f32_e32 v69, 1.0, v69
	v_rcp_f32_e32 v70, v69
	v_mul_f32_e32 v69, 0x3d372713, v42
	v_fma_f32 v69, v42, v69, 1.0
	v_mul_f32_e32 v69, v42, v69
	v_mul_f32_e32 v69, 0xc0135761, v69
	v_exp_f32_e32 v69, v69
	s_nop 0
	v_add_f32_e32 v69, 1.0, v69
	v_rcp_f32_e32 v72, v69
	v_mul_f32_e32 v69, 0x3d372713, v47
	v_fma_f32 v69, v47, v69, 1.0
	v_mul_f32_e32 v69, v47, v69
	v_mul_f32_e32 v69, 0xc0135761, v69
	v_exp_f32_e32 v69, v69
	s_nop 0
	v_add_f32_e32 v69, 1.0, v69
	v_rcp_f32_e32 v71, v69
	s_nop 0
	v_pk_mul_f32 v[70:71], v[46:47], v[70:71]
	v_mul_f32_e32 v46, 0x3d372713, v43
	v_fma_f32 v46, v43, v46, 1.0
	v_mul_f32_e32 v46, v43, v46
	v_mul_f32_e32 v46, 0xc0135761, v46
	v_exp_f32_e32 v46, v46
	v_cvt_pk_bf16_f32 v69, v70, v71
	v_pk_add_f32 v[34:35], v[34:35], v[68:69] op_sel_hi:[1,0]
	v_pk_add_f32 v[38:39], v[38:39], v[68:69] op_sel_hi:[1,0]
	v_add_f32_e32 v46, 1.0, v46
	v_rcp_f32_e32 v73, v46
	v_pk_add_f32 v[36:37], v[36:37], v[68:69] op_sel_hi:[1,0]
	v_pk_add_f32 v[40:41], v[40:41], v[68:69] op_sel_hi:[1,0]
	v_pk_mul_f32 v[72:73], v[42:43], v[72:73]
	v_mul_f32_e32 v43, 0x3d372713, v44
	v_fma_f32 v43, v44, v43, 1.0
	v_mul_f32_e32 v43, v44, v43
	v_mul_f32_e32 v43, 0xc0135761, v43
	v_exp_f32_e32 v43, v43
	v_mul_f32_e32 v42, 0x3d372713, v48
	v_fma_f32 v42, v48, v42, 1.0
	v_mul_f32_e32 v42, v48, v42
	v_add_f32_e32 v43, 1.0, v43
	v_rcp_f32_e32 v46, v43
	v_mul_f32_e32 v43, 0x3d372713, v49
	v_fma_f32 v43, v49, v43, 1.0
	v_mul_f32_e32 v43, v49, v43
	v_mul_f32_e32 v42, 0xc0135761, v42
	v_mul_f32_e32 v43, 0xc0135761, v43
	v_exp_f32_e32 v42, v42
	v_exp_f32_e32 v43, v43
	v_add_f32_e32 v42, 1.0, v42
	v_add_f32_e32 v43, 1.0, v43
	v_rcp_f32_e32 v42, v42
	v_rcp_f32_e32 v43, v43
	s_nop 0
	v_pk_mul_f32 v[74:75], v[48:49], v[42:43]
	v_mul_f32_e32 v42, 0x3d372713, v45
	v_fma_f32 v42, v45, v42, 1.0
	v_mul_f32_e32 v42, v45, v42
	v_mul_f32_e32 v42, 0xc0135761, v42
	v_exp_f32_e32 v42, v42
	v_pk_fma_f32 v[48:49], v[72:73], v[72:73], v[60:61]
	v_add_f32_e32 v42, 1.0, v42
	v_rcp_f32_e32 v47, v42
	v_pk_fma_f32 v[42:43], v[74:75], v[74:75], v[62:63]
	v_pk_mul_f32 v[76:77], v[44:45], v[46:47]
	v_pk_fma_f32 v[46:47], v[70:71], v[70:71], v[58:59]
	v_mul_f32_e32 v59, 0x3d372713, v34
	v_fma_f32 v59, v34, v59, 1.0
	v_mul_f32_e32 v59, v34, v59
	v_mul_f32_e32 v59, 0xc0135761, v59
	v_exp_f32_e32 v59, v59
	v_mul_f32_e32 v58, 0x3d372713, v38
	v_fma_f32 v58, v38, v58, 1.0
	v_mul_f32_e32 v58, v38, v58
	v_add_f32_e32 v59, 1.0, v59
	v_rcp_f32_e32 v60, v59
	v_mul_f32_e32 v59, 0x3d372713, v39
	v_fma_f32 v59, v39, v59, 1.0
	v_mul_f32_e32 v59, v39, v59
	v_mul_f32_e32 v58, 0xc0135761, v58
	v_mul_f32_e32 v59, 0xc0135761, v59
	v_exp_f32_e32 v58, v58
	v_exp_f32_e32 v59, v59
	v_pk_fma_f32 v[44:45], v[76:77], v[76:77], v[64:65]
	v_cvt_pk_bf16_f32 v70, v74, v75
	v_add_f32_e32 v58, 1.0, v58
	v_add_f32_e32 v59, 1.0, v59
	v_rcp_f32_e32 v58, v58
	v_rcp_f32_e32 v59, v59
	v_cvt_pk_bf16_f32 v71, v72, v73
	v_cvt_pk_bf16_f32 v72, v76, v77
	v_pk_mul_f32 v[58:59], v[38:39], v[58:59]
	v_mul_f32_e32 v38, 0x3d372713, v35
	v_fma_f32 v38, v35, v38, 1.0
	v_mul_f32_e32 v38, v35, v38
	v_mul_f32_e32 v38, 0xc0135761, v38
	v_exp_f32_e32 v38, v38
	s_nop 0
	v_add_f32_e32 v38, 1.0, v38
	v_rcp_f32_e32 v61, v38
	s_nop 0
	v_pk_mul_f32 v[60:61], v[34:35], v[60:61]
	v_mul_f32_e32 v35, 0x3d372713, v36
	v_fma_f32 v35, v36, v35, 1.0
	v_mul_f32_e32 v35, v36, v35
	v_mul_f32_e32 v35, 0xc0135761, v35
	v_exp_f32_e32 v35, v35
	v_mul_f32_e32 v34, 0x3d372713, v40
	v_fma_f32 v34, v40, v34, 1.0
	v_mul_f32_e32 v34, v40, v34
	v_add_f32_e32 v35, 1.0, v35
	v_rcp_f32_e32 v38, v35
	v_mul_f32_e32 v35, 0x3d372713, v41
	v_fma_f32 v35, v41, v35, 1.0
	v_mul_f32_e32 v35, v41, v35
	v_mul_f32_e32 v34, 0xc0135761, v34
	v_mul_f32_e32 v35, 0xc0135761, v35
	v_exp_f32_e32 v34, v34
	v_exp_f32_e32 v35, v35
	v_add_f32_e32 v34, 1.0, v34
	v_add_f32_e32 v35, 1.0, v35
	v_rcp_f32_e32 v34, v34
	v_rcp_f32_e32 v35, v35
	s_nop 0
	v_pk_mul_f32 v[62:63], v[40:41], v[34:35]
	v_mul_f32_e32 v34, 0x3d372713, v37
	v_fma_f32 v34, v37, v34, 1.0
	v_mul_f32_e32 v34, v37, v34
	v_mul_f32_e32 v34, 0xc0135761, v34
	v_exp_f32_e32 v34, v34
	v_pk_fma_f32 v[40:41], v[60:61], v[60:61], v[52:53]
	v_cvt_pk_bf16_f32 v52, v60, v61
	v_add_f32_e32 v34, 1.0, v34
	v_rcp_f32_e32 v39, v34
	v_pk_fma_f32 v[34:35], v[62:63], v[62:63], v[54:55]
	v_mov_b32_e32 v54, v69
	v_mov_b32_e32 v55, v70
	v_pk_mul_f32 v[64:65], v[36:37], v[38:39]
	v_pk_fma_f32 v[38:39], v[58:59], v[58:59], v[50:51]
	v_pk_fma_f32 v[36:37], v[64:65], v[64:65], v[56:57]
	v_cvt_pk_bf16_f32 v50, v58, v59
	v_cvt_pk_bf16_f32 v51, v62, v63
	v_cvt_pk_bf16_f32 v53, v64, v65
	v_mov_b32_e32 v56, v71
	v_mov_b32_e32 v57, v72
	v_mov_b32_dpp v54, v50 row_ror:8 row_mask:0xf bank_mask:0xc
	v_mov_b32_dpp v55, v51 row_ror:8 row_mask:0xf bank_mask:0xc
	v_mov_b32_dpp v56, v52 row_ror:8 row_mask:0xf bank_mask:0xc
	v_mov_b32_dpp v57, v53 row_ror:8 row_mask:0xf bank_mask:0xc
	v_mov_b32_dpp v50, v69 row_ror:8 row_mask:0xf bank_mask:0x3
	v_mov_b32_dpp v51, v70 row_ror:8 row_mask:0xf bank_mask:0x3
	v_mov_b32_dpp v52, v71 row_ror:8 row_mask:0xf bank_mask:0x3
	v_mov_b32_dpp v53, v72 row_ror:8 row_mask:0xf bank_mask:0x3
	global_store_dwordx4 v[66:67], v[54:57], off
	global_store_dwordx4 v[66:67], v[50:53], off offset:2048
	s_nop 1
	v_mov_b32_e32 v50, v192
	v_pk_add_f32 v[30:31], v[30:31], v[50:51] op_sel_hi:[1,0]
	v_pk_add_f32 v[32:33], v[32:33], v[50:51] op_sel_hi:[1,0]
	v_pk_add_f32 v[28:29], v[28:29], v[50:51] op_sel_hi:[1,0]
	v_pk_add_f32 v[26:27], v[26:27], v[50:51] op_sel_hi:[1,0]
	v_mul_f32_e32 v51, 0x3d372713, v30
	v_fma_f32 v51, v30, v51, 1.0
	v_mul_f32_e32 v51, v30, v51
	v_mul_f32_e32 v51, 0xc0135761, v51
	v_exp_f32_e32 v51, v51
	s_nop 0
	v_add_f32_e32 v51, 1.0, v51
	v_rcp_f32_e32 v52, v51
	v_mul_f32_e32 v51, 0x3d372713, v26
	v_fma_f32 v51, v26, v51, 1.0
	v_mul_f32_e32 v51, v26, v51
	v_mul_f32_e32 v51, 0xc0135761, v51
	v_exp_f32_e32 v51, v51
	s_nop 0
	v_add_f32_e32 v51, 1.0, v51
	v_rcp_f32_e32 v54, v51
	v_mul_f32_e32 v51, 0x3d372713, v31
	v_fma_f32 v51, v31, v51, 1.0
	v_mul_f32_e32 v51, v31, v51
	v_mul_f32_e32 v51, 0xc0135761, v51
	v_exp_f32_e32 v51, v51
	s_nop 0
	v_add_f32_e32 v51, 1.0, v51
	v_rcp_f32_e32 v53, v51
	s_nop 0
	v_pk_mul_f32 v[52:53], v[30:31], v[52:53]
	v_mul_f32_e32 v30, 0x3d372713, v27
	v_fma_f32 v30, v27, v30, 1.0
	v_mul_f32_e32 v30, v27, v30
	v_mul_f32_e32 v30, 0xc0135761, v30
	v_exp_f32_e32 v30, v30
	v_cvt_pk_bf16_f32 v51, v52, v53
	v_pk_add_f32 v[18:19], v[18:19], v[50:51] op_sel_hi:[1,0]
	v_pk_add_f32 v[22:23], v[22:23], v[50:51] op_sel_hi:[1,0]
	v_add_f32_e32 v30, 1.0, v30
	v_rcp_f32_e32 v55, v30
	v_pk_add_f32 v[20:21], v[20:21], v[50:51] op_sel_hi:[1,0]
	v_pk_add_f32 v[24:25], v[24:25], v[50:51] op_sel_hi:[1,0]
	v_pk_mul_f32 v[54:55], v[26:27], v[54:55]
	v_mul_f32_e32 v27, 0x3d372713, v28
	v_fma_f32 v27, v28, v27, 1.0
	v_mul_f32_e32 v27, v28, v27
	v_mul_f32_e32 v27, 0xc0135761, v27
	v_exp_f32_e32 v27, v27
	v_mul_f32_e32 v26, 0x3d372713, v32
	v_fma_f32 v26, v32, v26, 1.0
	v_mul_f32_e32 v26, v32, v26
	v_add_f32_e32 v27, 1.0, v27
	v_rcp_f32_e32 v30, v27
	v_mul_f32_e32 v27, 0x3d372713, v33
	v_fma_f32 v27, v33, v27, 1.0
	v_mul_f32_e32 v27, v33, v27
	v_mul_f32_e32 v26, 0xc0135761, v26
	v_mul_f32_e32 v27, 0xc0135761, v27
	v_exp_f32_e32 v26, v26
	v_exp_f32_e32 v27, v27
	v_add_f32_e32 v26, 1.0, v26
	v_add_f32_e32 v27, 1.0, v27
	v_rcp_f32_e32 v26, v26
	v_rcp_f32_e32 v27, v27
	s_nop 0
	v_pk_mul_f32 v[56:57], v[32:33], v[26:27]
	v_mul_f32_e32 v26, 0x3d372713, v29
	v_fma_f32 v26, v29, v26, 1.0
	v_mul_f32_e32 v26, v29, v26
	v_mul_f32_e32 v26, 0xc0135761, v26
	v_exp_f32_e32 v26, v26
	s_nop 0
	v_add_f32_e32 v26, 1.0, v26
	v_rcp_f32_e32 v31, v26
	v_pk_fma_f32 v[26:27], v[52:53], v[52:53], v[46:47]
	v_cvt_pk_bf16_f32 v52, v56, v57
	v_cvt_pk_bf16_f32 v53, v54, v55
	v_pk_mul_f32 v[58:59], v[28:29], v[30:31]
	v_pk_fma_f32 v[30:31], v[56:57], v[56:57], v[42:43]
	v_mul_f32_e32 v43, 0x3d372713, v18
	v_fma_f32 v43, v18, v43, 1.0
	v_mul_f32_e32 v43, v18, v43
	v_mul_f32_e32 v43, 0xc0135761, v43
	v_exp_f32_e32 v43, v43
	v_pk_fma_f32 v[32:33], v[58:59], v[58:59], v[44:45]
	v_mul_f32_e32 v42, 0x3d372713, v22
	v_fma_f32 v42, v22, v42, 1.0
	v_add_f32_e32 v43, 1.0, v43
	v_rcp_f32_e32 v44, v43
	v_mul_f32_e32 v43, 0x3d372713, v23
	v_fma_f32 v43, v23, v43, 1.0
	v_mul_f32_e32 v42, v22, v42
	v_mul_f32_e32 v43, v23, v43
	v_mul_f32_e32 v42, 0xc0135761, v42
	v_mul_f32_e32 v43, 0xc0135761, v43
	v_exp_f32_e32 v42, v42
	v_exp_f32_e32 v43, v43
	v_pk_fma_f32 v[28:29], v[54:55], v[54:55], v[48:49]
	v_cvt_pk_bf16_f32 v54, v58, v59
	v_add_f32_e32 v42, 1.0, v42
	v_add_f32_e32 v43, 1.0, v43
	v_rcp_f32_e32 v42, v42
	v_rcp_f32_e32 v43, v43
	s_nop 0
	v_pk_mul_f32 v[42:43], v[22:23], v[42:43]
	v_mul_f32_e32 v22, 0x3d372713, v19
	v_fma_f32 v22, v19, v22, 1.0
	v_mul_f32_e32 v22, v19, v22
	v_mul_f32_e32 v22, 0xc0135761, v22
	v_exp_f32_e32 v22, v22
	s_nop 0
	v_add_f32_e32 v22, 1.0, v22
	v_rcp_f32_e32 v45, v22
	s_nop 0
	v_pk_mul_f32 v[44:45], v[18:19], v[44:45]
	v_mul_f32_e32 v19, 0x3d372713, v20
	v_fma_f32 v19, v20, v19, 1.0
	v_mul_f32_e32 v19, v20, v19
	v_mul_f32_e32 v19, 0xc0135761, v19
	v_exp_f32_e32 v19, v19
	v_mul_f32_e32 v18, 0x3d372713, v24
	v_fma_f32 v18, v24, v18, 1.0
	v_mul_f32_e32 v18, v24, v18
	v_add_f32_e32 v19, 1.0, v19
	v_rcp_f32_e32 v22, v19
	v_mul_f32_e32 v19, 0x3d372713, v25
	v_fma_f32 v19, v25, v19, 1.0
	v_mul_f32_e32 v19, v25, v19
	v_mul_f32_e32 v18, 0xc0135761, v18
	v_mul_f32_e32 v19, 0xc0135761, v19
	v_exp_f32_e32 v18, v18
	v_exp_f32_e32 v19, v19
	v_add_f32_e32 v18, 1.0, v18
	v_add_f32_e32 v19, 1.0, v19
	v_rcp_f32_e32 v18, v18
	v_rcp_f32_e32 v19, v19
	s_nop 0
	v_pk_mul_f32 v[46:47], v[24:25], v[18:19]
	v_mul_f32_e32 v18, 0x3d372713, v21
	v_fma_f32 v18, v21, v18, 1.0
	v_mul_f32_e32 v18, v21, v18
	v_mul_f32_e32 v18, 0xc0135761, v18
	v_exp_f32_e32 v18, v18
	s_nop 0
	v_add_f32_e32 v18, 1.0, v18
	v_rcp_f32_e32 v23, v18
	v_pk_fma_f32 v[18:19], v[42:43], v[42:43], v[38:39]
	v_cvt_pk_bf16_f32 v38, v44, v45
	v_pk_mul_f32 v[48:49], v[20:21], v[22:23]
	v_pk_fma_f32 v[20:21], v[44:45], v[44:45], v[40:41]
	v_add_co_u32_e32 v44, vcc, s0, v130
	s_mov_b32 s0, 0xb000
	s_nop 0
	v_addc_co_u32_e32 v45, vcc, 0, v131, vcc
	v_pk_fma_f32 v[22:23], v[46:47], v[46:47], v[34:35]
	v_pk_fma_f32 v[24:25], v[48:49], v[48:49], v[36:37]
	v_cvt_pk_bf16_f32 v36, v42, v43
	v_cvt_pk_bf16_f32 v37, v46, v47
	v_cvt_pk_bf16_f32 v39, v48, v49
	v_mov_b32_e32 v40, v51
	v_mov_b32_e32 v41, v52
	v_mov_b32_e32 v42, v53
	v_mov_b32_e32 v43, v54
	v_add_co_u32_e32 v34, vcc, s0, v130
	v_mov_b32_dpp v40, v36 row_ror:8 row_mask:0xf bank_mask:0xc
	v_mov_b32_dpp v41, v37 row_ror:8 row_mask:0xf bank_mask:0xc
	v_mov_b32_dpp v42, v38 row_ror:8 row_mask:0xf bank_mask:0xc
	v_mov_b32_dpp v43, v39 row_ror:8 row_mask:0xf bank_mask:0xc
	v_addc_co_u32_e32 v35, vcc, 0, v131, vcc
	v_mov_b32_dpp v36, v51 row_ror:8 row_mask:0xf bank_mask:0x3
	v_mov_b32_dpp v37, v52 row_ror:8 row_mask:0xf bank_mask:0x3
	v_mov_b32_dpp v38, v53 row_ror:8 row_mask:0xf bank_mask:0x3
	v_mov_b32_dpp v39, v54 row_ror:8 row_mask:0xf bank_mask:0x3
	global_store_dwordx4 v[34:35], v[40:43], off offset:-4096
	global_store_dwordx4 v[44:45], v[36:39], off offset:2048
	s_nop 1
	v_mov_b32_e32 v36, v193
	v_cmp_eq_u32_e32 vcc, 0, v142
	v_pk_add_f32 v[14:15], v[14:15], v[36:37] op_sel_hi:[1,0]
	v_pk_add_f32 v[16:17], v[16:17], v[36:37] op_sel_hi:[1,0]
	v_pk_add_f32 v[12:13], v[12:13], v[36:37] op_sel_hi:[1,0]
	v_pk_add_f32 v[10:11], v[10:11], v[36:37] op_sel_hi:[1,0]
	v_mul_f32_e32 v37, 0x3d372713, v14
	v_fma_f32 v37, v14, v37, 1.0
	v_mul_f32_e32 v37, v14, v37
	v_mul_f32_e32 v37, 0xc0135761, v37
	v_exp_f32_e32 v37, v37
	s_nop 0
	v_add_f32_e32 v37, 1.0, v37
	v_rcp_f32_e32 v38, v37
	v_mul_f32_e32 v37, 0x3d372713, v10
	v_fma_f32 v37, v10, v37, 1.0
	v_mul_f32_e32 v37, v10, v37
	v_mul_f32_e32 v37, 0xc0135761, v37
	v_exp_f32_e32 v37, v37
	s_nop 0
	v_add_f32_e32 v37, 1.0, v37
	v_rcp_f32_e32 v40, v37
	v_mul_f32_e32 v37, 0x3d372713, v15
	v_fma_f32 v37, v15, v37, 1.0
	v_mul_f32_e32 v37, v15, v37
	v_mul_f32_e32 v37, 0xc0135761, v37
	v_exp_f32_e32 v37, v37
	s_nop 0
	v_add_f32_e32 v37, 1.0, v37
	v_rcp_f32_e32 v39, v37
	s_nop 0
	v_pk_mul_f32 v[38:39], v[14:15], v[38:39]
	v_mul_f32_e32 v14, 0x3d372713, v11
	v_fma_f32 v14, v11, v14, 1.0
	v_mul_f32_e32 v14, v11, v14
	v_mul_f32_e32 v14, 0xc0135761, v14
	v_exp_f32_e32 v14, v14
	v_cvt_pk_bf16_f32 v37, v38, v39
	v_pk_add_f32 v[2:3], v[2:3], v[36:37] op_sel_hi:[1,0]
	v_pk_fma_f32 v[26:27], v[38:39], v[38:39], v[26:27]
	v_add_f32_e32 v14, 1.0, v14
	v_rcp_f32_e32 v41, v14
	v_pk_add_f32 v[6:7], v[6:7], v[36:37] op_sel_hi:[1,0]
	v_pk_add_f32 v[4:5], v[4:5], v[36:37] op_sel_hi:[1,0]
	v_pk_add_f32 v[8:9], v[8:9], v[36:37] op_sel_hi:[1,0]
	v_pk_mul_f32 v[40:41], v[10:11], v[40:41]
	v_mul_f32_e32 v11, 0x3d372713, v12
	v_fma_f32 v11, v12, v11, 1.0
	v_mul_f32_e32 v11, v12, v11
	v_mul_f32_e32 v11, 0xc0135761, v11
	v_exp_f32_e32 v11, v11
	v_mul_f32_e32 v10, 0x3d372713, v16
	v_fma_f32 v10, v16, v10, 1.0
	v_mul_f32_e32 v10, v16, v10
	v_add_f32_e32 v11, 1.0, v11
	v_rcp_f32_e32 v14, v11
	v_mul_f32_e32 v11, 0x3d372713, v17
	v_fma_f32 v11, v17, v11, 1.0
	v_mul_f32_e32 v11, v17, v11
	v_mul_f32_e32 v10, 0xc0135761, v10
	v_mul_f32_e32 v11, 0xc0135761, v11
	v_exp_f32_e32 v10, v10
	v_exp_f32_e32 v11, v11
	v_cvt_pk_bf16_f32 v39, v40, v41
	v_add_f32_e32 v10, 1.0, v10
	v_add_f32_e32 v11, 1.0, v11
	v_rcp_f32_e32 v10, v10
	v_rcp_f32_e32 v11, v11
	s_nop 0
	v_pk_mul_f32 v[16:17], v[16:17], v[10:11]
	v_mul_f32_e32 v10, 0x3d372713, v13
	v_fma_f32 v10, v13, v10, 1.0
	v_mul_f32_e32 v10, v13, v10
	v_mul_f32_e32 v10, 0xc0135761, v10
	v_exp_f32_e32 v10, v10
	v_cvt_pk_bf16_f32 v38, v16, v17
	v_add_f32_e32 v10, 1.0, v10
	v_rcp_f32_e32 v15, v10
	s_nop 0
	v_pk_mul_f32 v[42:43], v[12:13], v[14:15]
	v_pk_fma_f32 v[14:15], v[16:17], v[16:17], v[30:31]
	v_mul_f32_e32 v17, 0x3d372713, v2
	v_fma_f32 v17, v2, v17, 1.0
	v_mul_f32_e32 v17, v2, v17
	v_mul_f32_e32 v17, 0xc0135761, v17
	v_exp_f32_e32 v17, v17
	v_pk_fma_f32 v[12:13], v[40:41], v[40:41], v[28:29]
	v_mul_f32_e32 v16, 0x3d372713, v6
	v_fma_f32 v16, v6, v16, 1.0
	v_add_f32_e32 v17, 1.0, v17
	v_rcp_f32_e32 v28, v17
	v_mul_f32_e32 v17, 0x3d372713, v7
	v_fma_f32 v17, v7, v17, 1.0
	v_mul_f32_e32 v16, v6, v16
	v_mul_f32_e32 v17, v7, v17
	v_mul_f32_e32 v16, 0xc0135761, v16
	v_mul_f32_e32 v17, 0xc0135761, v17
	v_exp_f32_e32 v16, v16
	v_exp_f32_e32 v17, v17
	v_cvt_pk_bf16_f32 v40, v42, v43
	v_pk_fma_f32 v[10:11], v[42:43], v[42:43], v[32:33]
	v_add_f32_e32 v16, 1.0, v16
	v_add_f32_e32 v17, 1.0, v17
	v_rcp_f32_e32 v16, v16
	v_rcp_f32_e32 v17, v17
	s_nop 0
	v_pk_mul_f32 v[6:7], v[6:7], v[16:17]
	v_mul_f32_e32 v16, 0x3d372713, v3
	v_fma_f32 v16, v3, v16, 1.0
	v_mul_f32_e32 v16, v3, v16
	v_mul_f32_e32 v16, 0xc0135761, v16
	v_exp_f32_e32 v16, v16
	v_pk_fma_f32 v[18:19], v[6:7], v[6:7], v[18:19]
	v_add_f32_e32 v16, 1.0, v16
	v_rcp_f32_e32 v29, v16
	s_nop 0
	v_pk_mul_f32 v[16:17], v[2:3], v[28:29]
	v_mul_f32_e32 v3, 0x3d372713, v4
	v_fma_f32 v3, v4, v3, 1.0
	v_mul_f32_e32 v3, v4, v3
	v_mul_f32_e32 v3, 0xc0135761, v3
	v_exp_f32_e32 v3, v3
	v_mul_f32_e32 v2, 0x3d372713, v8
	v_fma_f32 v2, v8, v2, 1.0
	v_mul_f32_e32 v2, v8, v2
	v_add_f32_e32 v3, 1.0, v3
	v_rcp_f32_e32 v28, v3
	v_mul_f32_e32 v3, 0x3d372713, v9
	v_fma_f32 v3, v9, v3, 1.0
	v_mul_f32_e32 v3, v9, v3
	v_mul_f32_e32 v2, 0xc0135761, v2
	v_mul_f32_e32 v3, 0xc0135761, v3
	v_exp_f32_e32 v2, v2
	v_exp_f32_e32 v3, v3
	v_pk_fma_f32 v[32:33], v[16:17], v[16:17], v[20:21]
	v_mov_b32_dpp v20, v18 quad_perm:[1,0,3,2] row_mask:0xf bank_mask:0xf bound_ctrl:1
	v_add_f32_e32 v2, 1.0, v2
	v_add_f32_e32 v3, 1.0, v3
	v_rcp_f32_e32 v2, v2
	v_rcp_f32_e32 v3, v3
	v_mov_b32_dpp v21, v19 quad_perm:[1,0,3,2] row_mask:0xf bank_mask:0xf bound_ctrl:1
	v_pk_add_f32 v[18:19], v[18:19], v[20:21]
	v_pk_mul_f32 v[8:9], v[8:9], v[2:3]
	v_mul_f32_e32 v2, 0x3d372713, v5
	v_fma_f32 v2, v5, v2, 1.0
	v_mul_f32_e32 v2, v5, v2
	v_mul_f32_e32 v2, 0xc0135761, v2
	v_exp_f32_e32 v2, v2
	v_pk_fma_f32 v[22:23], v[8:9], v[8:9], v[22:23]
	v_cvt_pk_bf16_f32 v3, v8, v9
	v_mov_b32_e32 v8, v39
	v_add_f32_e32 v2, 1.0, v2
	v_rcp_f32_e32 v29, v2
	v_cvt_pk_bf16_f32 v2, v6, v7
	v_mov_b32_e32 v6, v37
	v_mov_b32_e32 v7, v38
	v_pk_mul_f32 v[28:29], v[4:5], v[28:29]
	v_cvt_pk_bf16_f32 v4, v16, v17
	v_cvt_pk_bf16_f32 v5, v28, v29
	v_mov_b32_e32 v9, v40
	v_mov_b32_dpp v6, v2 row_ror:8 row_mask:0xf bank_mask:0xc
	v_mov_b32_dpp v2, v37 row_ror:8 row_mask:0xf bank_mask:0x3
	v_mov_b32_dpp v7, v3 row_ror:8 row_mask:0xf bank_mask:0xc
	v_mov_b32_dpp v3, v38 row_ror:8 row_mask:0xf bank_mask:0x3
	v_mov_b32_dpp v8, v4 row_ror:8 row_mask:0xf bank_mask:0xc
	v_mov_b32_dpp v9, v5 row_ror:8 row_mask:0xf bank_mask:0xc
	v_mov_b32_dpp v4, v39 row_ror:8 row_mask:0xf bank_mask:0x3
	v_mov_b32_dpp v5, v40 row_ror:8 row_mask:0xf bank_mask:0x3
	global_store_dwordx4 v[34:35], v[6:9], off
	global_store_dwordx4 v[34:35], v[2:5], off offset:2048
	v_pk_fma_f32 v[30:31], v[28:29], v[28:29], v[24:25]
	v_mov_b32_dpp v6, v14 quad_perm:[1,0,3,2] row_mask:0xf bank_mask:0xf bound_ctrl:1
	v_mov_b32_dpp v2, v26 quad_perm:[1,0,3,2] row_mask:0xf bank_mask:0xf bound_ctrl:1
	v_mov_b32_dpp v3, v27 quad_perm:[1,0,3,2] row_mask:0xf bank_mask:0xf bound_ctrl:1
	v_pk_add_f32 v[2:3], v[26:27], v[2:3]
	v_mov_b32_dpp v7, v15 quad_perm:[1,0,3,2] row_mask:0xf bank_mask:0xf bound_ctrl:1
	v_mov_b32_dpp v26, v32 quad_perm:[1,0,3,2] row_mask:0xf bank_mask:0xf bound_ctrl:1
	v_mov_b32_dpp v27, v33 quad_perm:[1,0,3,2] row_mask:0xf bank_mask:0xf bound_ctrl:1
	v_pk_add_f32 v[6:7], v[14:15], v[6:7]
	v_mov_b32_dpp v14, v12 quad_perm:[1,0,3,2] row_mask:0xf bank_mask:0xf bound_ctrl:1
	v_mov_b32_dpp v15, v13 quad_perm:[1,0,3,2] row_mask:0xf bank_mask:0xf bound_ctrl:1
	v_mov_b32_dpp v16, v10 quad_perm:[1,0,3,2] row_mask:0xf bank_mask:0xf bound_ctrl:1
	v_mov_b32_dpp v17, v11 quad_perm:[1,0,3,2] row_mask:0xf bank_mask:0xf bound_ctrl:1
	v_mov_b32_dpp v24, v22 quad_perm:[1,0,3,2] row_mask:0xf bank_mask:0xf bound_ctrl:1
	v_mov_b32_dpp v25, v23 quad_perm:[1,0,3,2] row_mask:0xf bank_mask:0xf bound_ctrl:1
	v_pk_add_f32 v[26:27], v[32:33], v[26:27]
	v_mov_b32_dpp v32, v30 quad_perm:[1,0,3,2] row_mask:0xf bank_mask:0xf bound_ctrl:1
	v_mov_b32_dpp v33, v31 quad_perm:[1,0,3,2] row_mask:0xf bank_mask:0xf bound_ctrl:1
	v_pk_add_f32 v[12:13], v[12:13], v[14:15]
	v_pk_add_f32 v[10:11], v[10:11], v[16:17]
	v_pk_add_f32 v[22:23], v[22:23], v[24:25]
	v_pk_add_f32 v[30:31], v[30:31], v[32:33]
	v_mov_b32_dpp v4, v2 quad_perm:[2,3,0,1] row_mask:0xf bank_mask:0xf bound_ctrl:1
	v_mov_b32_dpp v5, v3 quad_perm:[2,3,0,1] row_mask:0xf bank_mask:0xf bound_ctrl:1
	v_mov_b32_dpp v8, v6 quad_perm:[2,3,0,1] row_mask:0xf bank_mask:0xf bound_ctrl:1
	v_mov_b32_dpp v9, v7 quad_perm:[2,3,0,1] row_mask:0xf bank_mask:0xf bound_ctrl:1
	v_mov_b32_dpp v14, v12 quad_perm:[2,3,0,1] row_mask:0xf bank_mask:0xf bound_ctrl:1
	v_mov_b32_dpp v15, v13 quad_perm:[2,3,0,1] row_mask:0xf bank_mask:0xf bound_ctrl:1
	v_mov_b32_dpp v16, v10 quad_perm:[2,3,0,1] row_mask:0xf bank_mask:0xf bound_ctrl:1
	v_mov_b32_dpp v17, v11 quad_perm:[2,3,0,1] row_mask:0xf bank_mask:0xf bound_ctrl:1
	v_mov_b32_dpp v20, v18 quad_perm:[2,3,0,1] row_mask:0xf bank_mask:0xf bound_ctrl:1
	v_mov_b32_dpp v21, v19 quad_perm:[2,3,0,1] row_mask:0xf bank_mask:0xf bound_ctrl:1
	v_mov_b32_dpp v24, v22 quad_perm:[2,3,0,1] row_mask:0xf bank_mask:0xf bound_ctrl:1
	v_mov_b32_dpp v25, v23 quad_perm:[2,3,0,1] row_mask:0xf bank_mask:0xf bound_ctrl:1
	v_mov_b32_dpp v28, v26 quad_perm:[2,3,0,1] row_mask:0xf bank_mask:0xf bound_ctrl:1
	v_mov_b32_dpp v29, v27 quad_perm:[2,3,0,1] row_mask:0xf bank_mask:0xf bound_ctrl:1
	v_mov_b32_dpp v32, v30 quad_perm:[2,3,0,1] row_mask:0xf bank_mask:0xf bound_ctrl:1
	v_mov_b32_dpp v33, v31 quad_perm:[2,3,0,1] row_mask:0xf bank_mask:0xf bound_ctrl:1
	v_pk_add_f32 v[2:3], v[2:3], v[4:5]
	v_pk_add_f32 v[6:7], v[6:7], v[8:9]
	v_pk_add_f32 v[12:13], v[12:13], v[14:15]
	v_pk_add_f32 v[10:11], v[10:11], v[16:17]
	v_pk_add_f32 v[18:19], v[18:19], v[20:21]
	v_pk_add_f32 v[22:23], v[22:23], v[24:25]
	v_pk_add_f32 v[26:27], v[26:27], v[28:29]
	v_pk_add_f32 v[30:31], v[30:31], v[32:33]
	v_mov_b32_dpp v4, v2 row_half_mirror row_mask:0xf bank_mask:0xf bound_ctrl:1
	v_mov_b32_dpp v5, v3 row_half_mirror row_mask:0xf bank_mask:0xf bound_ctrl:1
	v_mov_b32_dpp v8, v6 row_half_mirror row_mask:0xf bank_mask:0xf bound_ctrl:1
	v_mov_b32_dpp v9, v7 row_half_mirror row_mask:0xf bank_mask:0xf bound_ctrl:1
	v_mov_b32_dpp v14, v12 row_half_mirror row_mask:0xf bank_mask:0xf bound_ctrl:1
	v_mov_b32_dpp v15, v13 row_half_mirror row_mask:0xf bank_mask:0xf bound_ctrl:1
	v_mov_b32_dpp v16, v10 row_half_mirror row_mask:0xf bank_mask:0xf bound_ctrl:1
	v_mov_b32_dpp v17, v11 row_half_mirror row_mask:0xf bank_mask:0xf bound_ctrl:1
	v_mov_b32_dpp v20, v18 row_half_mirror row_mask:0xf bank_mask:0xf bound_ctrl:1
	v_mov_b32_dpp v21, v19 row_half_mirror row_mask:0xf bank_mask:0xf bound_ctrl:1
	v_mov_b32_dpp v24, v22 row_half_mirror row_mask:0xf bank_mask:0xf bound_ctrl:1
	v_mov_b32_dpp v25, v23 row_half_mirror row_mask:0xf bank_mask:0xf bound_ctrl:1
	v_mov_b32_dpp v28, v26 row_half_mirror row_mask:0xf bank_mask:0xf bound_ctrl:1
	v_mov_b32_dpp v29, v27 row_half_mirror row_mask:0xf bank_mask:0xf bound_ctrl:1
	v_mov_b32_dpp v32, v30 row_half_mirror row_mask:0xf bank_mask:0xf bound_ctrl:1
	v_mov_b32_dpp v33, v31 row_half_mirror row_mask:0xf bank_mask:0xf bound_ctrl:1
	v_pk_add_f32 v[2:3], v[2:3], v[4:5]
	v_pk_add_f32 v[6:7], v[6:7], v[8:9]
	v_pk_add_f32 v[12:13], v[12:13], v[14:15]
	v_pk_add_f32 v[10:11], v[10:11], v[16:17]
	v_pk_add_f32 v[18:19], v[18:19], v[20:21]
	v_pk_add_f32 v[22:23], v[22:23], v[24:25]
	v_pk_add_f32 v[26:27], v[26:27], v[28:29]
	v_pk_add_f32 v[30:31], v[30:31], v[32:33]
	v_mov_b32_dpp v4, v2 row_mirror row_mask:0xf bank_mask:0xf bound_ctrl:1
	v_mov_b32_dpp v5, v3 row_mirror row_mask:0xf bank_mask:0xf bound_ctrl:1
	v_mov_b32_dpp v8, v6 row_mirror row_mask:0xf bank_mask:0xf bound_ctrl:1
	v_mov_b32_dpp v9, v7 row_mirror row_mask:0xf bank_mask:0xf bound_ctrl:1
	v_mov_b32_dpp v14, v12 row_mirror row_mask:0xf bank_mask:0xf bound_ctrl:1
	v_mov_b32_dpp v15, v13 row_mirror row_mask:0xf bank_mask:0xf bound_ctrl:1
	v_mov_b32_dpp v16, v10 row_mirror row_mask:0xf bank_mask:0xf bound_ctrl:1
	v_mov_b32_dpp v17, v11 row_mirror row_mask:0xf bank_mask:0xf bound_ctrl:1
	v_mov_b32_dpp v20, v18 row_mirror row_mask:0xf bank_mask:0xf bound_ctrl:1
	v_mov_b32_dpp v21, v19 row_mirror row_mask:0xf bank_mask:0xf bound_ctrl:1
	v_mov_b32_dpp v24, v22 row_mirror row_mask:0xf bank_mask:0xf bound_ctrl:1
	v_mov_b32_dpp v25, v23 row_mirror row_mask:0xf bank_mask:0xf bound_ctrl:1
	v_mov_b32_dpp v28, v26 row_mirror row_mask:0xf bank_mask:0xf bound_ctrl:1
	v_mov_b32_dpp v29, v27 row_mirror row_mask:0xf bank_mask:0xf bound_ctrl:1
	v_mov_b32_dpp v32, v30 row_mirror row_mask:0xf bank_mask:0xf bound_ctrl:1
	v_mov_b32_dpp v33, v31 row_mirror row_mask:0xf bank_mask:0xf bound_ctrl:1
	s_and_saveexec_b64 s[0:1], vcc
	s_cbranch_execz .LBB0_601
	s_lshl_b32 s5, s67, 1
	s_add_i32 s6, s5, s10
	s_lshl_b32 s4, s68, 8
	s_ashr_i32 s7, s6, 31
	s_or_b32 s4, s4, s64
	s_lshl_b64 s[6:7], s[6:7], 17
	s_add_u32 s6, s36, s6
	s_addc_u32 s7, s37, s7
	s_ashr_i32 s5, s4, 31
	s_lshl_b64 s[4:5], s[4:5], 2
	s_add_u32 s4, s6, s4
	v_pk_add_f32 v[6:7], v[6:7], v[8:9]
	v_pk_add_f32 v[4:5], v[2:3], v[4:5]
	s_addc_u32 s5, s7, s5
	v_lshlrev_b32_e32 v2, 2, v141
	v_pk_add_f32 v[30:31], v[30:31], v[32:33]
	v_pk_add_f32 v[28:29], v[26:27], v[28:29]
	v_pk_add_f32 v[22:23], v[22:23], v[24:25]
	v_pk_add_f32 v[20:21], v[18:19], v[20:21]
	v_pk_add_f32 v[16:17], v[10:11], v[16:17]
	v_pk_add_f32 v[14:15], v[12:13], v[14:15]
	global_store_dwordx4 v2, v[4:7], s[4:5]
	global_store_dwordx4 v2, v[14:17], s[4:5] offset:16
	global_store_dwordx4 v2, v[20:23], s[4:5] offset:128
	global_store_dwordx4 v2, v[28:31], s[4:5] offset:144
